# mixer SGU step B: cross-lane sums by DPP (quad_perm, row_half_mirror, row_mirror) with one ds_swizzle for the xor-16 step; the 16 u values of a lane loaded in one batch
# speedup vs baseline: 1.0076x; 1.0076x over previous
; __device__ __forceinline__ float bf16_lo(unsigned u) { return __uint_as_float(u << 16); }
; __device__ __forceinline__ float bf16_hi(unsigned u) { return __uint_as_float(u & 0xffff0000u); }
; #define SWZ_XOR(v, o) __int_as_float(__builtin_amdgcn_ds_swizzle(__float_as_int(v), ((o) << 10) | 0x1F))
; __device__ __forceinline__ float half_sum32(float v) {
;     v += SWZ_XOR(v, 16); v += SWZ_XOR(v, 8); v += SWZ_XOR(v, 4); v += SWZ_XOR(v, 2); v += SWZ_XOR(v, 1);
;     return v;
; __device__ __forceinline__ void phase_mixer(const Params& p, LAS3 char* lds, int wid) {
;     ...
;                 const bf16_t* ub = proj + (size_t)t0 * DIN + 3072 + hd * 128 + 4 * n + cp;
;                 float ya[16], yb[16];
; #pragma unroll
;                 for (int r = 0; r < 16; ++r) {
;                     const int tt = 32 * mt + (r & 3) + 8 * (r >> 2) + 4 * kh;
;                     const unsigned uu = *(const unsigned*)(ub + (size_t)tt * DIN);
;                     const float bias = p.sgu_b[hd * 128 + tt];
;                     ya[r] = gelu_f(bf16_lo(uu)) * (acc0[r] + bias);
;                     yb[r] = gelu_f(bf16_hi(uu)) * (acc1[r] + bias);
;                     const float ps = half_sum32(ya[r] * ya[r] + yb[r] * yb[r]);
;                     if (n == 0) stat[tt * 2 + (wid & 1)] = ps;
;                 }
.LBB0_179:
	s_mul_i32 s5, s94, 0x2800
	s_mul_hi_i32 s4, s94, 0x2800
	s_add_u32 s5, s56, s5
	s_addc_u32 s6, s57, s4
	s_lshl_b32 s10, s92, 1
	s_add_u32 s4, s5, s10
	s_addc_u32 s5, s6, 0
	v_lshl_add_u64 v[80:81], s[4:5], 0, v[36:37]
	s_lshl_b32 s26, s23, 1
	v_add_u32_e32 v82, s92, v94
	v_lshl_add_u64 v[80:81], v[80:81], 0, s[26:27]
	s_mov_b64 s[4:5], 0x1800
	v_ashrrev_i32_e32 v83, 31, v82
	v_lshl_add_u64 v[80:81], v[80:81], 0, s[4:5]
	v_lshl_add_u64 v[232:233], v[80:81], 0, v[40:41]
	global_load_dword v200, v[232:233], off
	v_lshl_add_u64 v[232:233], v[80:81], 0, v[42:43]
	global_load_dword v201, v[232:233], off
	v_lshl_add_u64 v[232:233], v[80:81], 0, v[44:45]
	global_load_dword v202, v[232:233], off
	v_lshl_add_u64 v[232:233], v[80:81], 0, v[46:47]
	global_load_dword v203, v[232:233], off
	v_lshl_add_u64 v[232:233], v[80:81], 0, v[48:49]
	global_load_dword v204, v[232:233], off
	v_lshl_add_u64 v[232:233], v[80:81], 0, v[50:51]
	global_load_dword v205, v[232:233], off
	v_lshl_add_u64 v[232:233], v[80:81], 0, v[52:53]
	global_load_dword v206, v[232:233], off
	v_lshl_add_u64 v[232:233], v[80:81], 0, v[54:55]
	global_load_dword v207, v[232:233], off
	v_lshl_add_u64 v[232:233], v[80:81], 0, v[56:57]
	global_load_dword v208, v[232:233], off
	v_lshl_add_u64 v[232:233], v[80:81], 0, v[62:63]
	global_load_dword v209, v[232:233], off
	v_lshl_add_u64 v[232:233], v[80:81], 0, v[64:65]
	global_load_dword v210, v[232:233], off
	v_lshl_add_u64 v[232:233], v[80:81], 0, v[66:67]
	global_load_dword v211, v[232:233], off
	v_lshl_add_u64 v[232:233], v[80:81], 0, v[68:69]
	global_load_dword v212, v[232:233], off
	v_lshl_add_u64 v[232:233], v[80:81], 0, v[70:71]
	global_load_dword v213, v[232:233], off
	v_lshl_add_u64 v[232:233], v[80:81], 0, v[72:73]
	global_load_dword v214, v[232:233], off
	v_lshl_add_u64 v[232:233], v[80:81], 0, v[74:75]
	global_load_dword v215, v[232:233], off
	v_lshl_add_u64 v[82:83], v[82:83], 2, s[98:99]
	global_load_dword v84, v[82:83], off
	v_lshl_add_u64 v[82:83], v[80:81], 0, v[40:41]
	s_waitcnt vmcnt(0)
	v_mov_b32_e32 v82, v200
	v_add_f32_e32 v16, v16, v84
	v_add_f32_e32 v0, v0, v84
	s_waitcnt vmcnt(0)
	v_lshlrev_b32_e32 v83, 16, v82
	v_and_b32_e32 v82, 0xffff0000, v82
	v_fma_f32 v84, |v83|, s87, 1.0
	v_fma_f32 v86, |v82|, s87, 1.0
	v_rcp_f32_e32 v84, v84
	v_rcp_f32_e32 v86, v86
	v_mul_f32_e32 v85, v83, v83
	v_mul_f32_e32 v87, v82, v82
	v_mul_f32_e32 v85, 0xbf38aa3b, v85
	v_fmamk_f32 v88, v84, 0x3f07dc22, v126
	v_mul_f32_e32 v87, 0xbf38aa3b, v87
	v_exp_f32_e32 v85, v85
	v_fmamk_f32 v89, v86, 0x3f07dc22, v126
	v_fmaak_f32 v88, v84, v88, 0x3f35f0e3
	v_exp_f32_e32 v87, v87
	v_fmaak_f32 v89, v86, v89, 0x3f35f0e3
	v_fmaak_f32 v88, v84, v88, 0xbe11a98e
	v_fmaak_f32 v89, v86, v89, 0xbe11a98e
	v_fmaak_f32 v88, v84, v88, 0x3e027906
	v_fmaak_f32 v89, v86, v89, 0x3e027906
	v_mul_f32_e32 v84, v84, v88
	v_mul_f32_e32 v86, v86, v89
	v_mul_f32_e32 v84, v85, v84
	v_mul_f32_e32 v85, v87, v86
	v_mul_f32_e32 v86, v84, v83
	v_fma_f32 v84, -v84, v83, v83
	v_cmp_gt_f32_e32 vcc, 0, v83
	v_mul_f32_e32 v87, v85, v82
	v_fma_f32 v85, -v85, v82, v82
	v_cndmask_b32_e32 v83, v84, v86, vcc
	v_cmp_gt_f32_e32 vcc, 0, v82
	v_mul_f32_e32 v16, v16, v83
	s_nop 0
	v_cndmask_b32_e32 v82, v85, v87, vcc
	v_mul_f32_e32 v84, v0, v82
	v_mul_f32_e32 v0, v84, v84
	v_fmac_f32_e32 v0, v16, v16
	s_nop 1
	s_waitcnt lgkmcnt(0)
	v_add_f32_dpp v0, v0, v0 quad_perm:[1,0,3,2] row_mask:0xf bank_mask:0xf
	s_nop 1
	s_waitcnt lgkmcnt(0)
	v_add_f32_dpp v0, v0, v0 quad_perm:[2,3,0,1] row_mask:0xf bank_mask:0xf
	s_nop 1
	s_waitcnt lgkmcnt(0)
	v_add_f32_dpp v0, v0, v0 row_half_mirror row_mask:0xf bank_mask:0xf
	s_nop 1
	s_waitcnt lgkmcnt(0)
	v_add_f32_dpp v0, v0, v0 row_mirror row_mask:0xf bank_mask:0xf
	ds_swizzle_b32 v82, v0 offset:swizzle(SWAP,16)
	s_and_saveexec_b64 s[4:5], s[0:1]
	s_cbranch_execz .LBB0_181
	s_waitcnt lgkmcnt(0)
	v_add_f32_e32 v0, v0, v82
	v_add_u32_e32 v82, s25, v95
	ds_write_b32 v82, v0 offset:32768
.LBB0_181:
	s_or_b64 exec, exec, s[4:5]
	s_waitcnt lgkmcnt(0)
	v_lshl_add_u64 v[82:83], v[80:81], 0, v[42:43]
	v_lshl_add_u64 v[82:83], s[92:93], 0, v[60:61]
	v_lshl_add_u64 v[82:83], v[82:83], 2, s[98:99]
	global_load_dword v85, v[82:83], off offset:4
	s_waitcnt vmcnt(0)
	v_mov_b32_e32 v0, v201
	v_lshlrev_b32_e32 v86, 16, v0
	v_and_b32_e32 v0, 0xffff0000, v0
	v_fma_f32 v87, |v86|, s87, 1.0
	v_mul_f32_e32 v88, v86, v86
	s_waitcnt vmcnt(0)
	v_add_f32_e32 v17, v17, v85
	v_fma_f32 v89, |v0|, s87, 1.0
	v_add_f32_e32 v1, v1, v85
	v_rcp_f32_e32 v85, v87
	v_mul_f32_e32 v87, 0xbf38aa3b, v88
	v_rcp_f32_e32 v88, v89
	v_mul_f32_e32 v90, v0, v0
	v_mul_f32_e32 v89, 0xbf38aa3b, v90
	v_fmamk_f32 v90, v85, 0x3f07dc22, v126
	v_exp_f32_e32 v87, v87
	v_fmamk_f32 v91, v88, 0x3f07dc22, v126
	v_fmaak_f32 v90, v85, v90, 0x3f35f0e3
	v_exp_f32_e32 v89, v89
	v_fmaak_f32 v91, v88, v91, 0x3f35f0e3
	v_fmaak_f32 v90, v85, v90, 0xbe11a98e
	v_fmaak_f32 v91, v88, v91, 0xbe11a98e
	v_fmaak_f32 v90, v85, v90, 0x3e027906
	v_fmaak_f32 v91, v88, v91, 0x3e027906
	v_mul_f32_e32 v85, v85, v90
	v_mul_f32_e32 v88, v88, v91
	v_mul_f32_e32 v85, v87, v85
	v_mul_f32_e32 v87, v89, v88
	v_mul_f32_e32 v88, v85, v86
	v_fma_f32 v85, -v85, v86, v86
	v_cmp_gt_f32_e32 vcc, 0, v86
	v_mul_f32_e32 v89, v87, v0
	v_fma_f32 v87, -v87, v0, v0
	v_cndmask_b32_e32 v85, v85, v88, vcc
	v_cmp_gt_f32_e32 vcc, 0, v0
	v_mul_f32_e32 v17, v17, v85
	s_nop 0
	v_cndmask_b32_e32 v0, v87, v89, vcc
	v_mul_f32_e32 v85, v1, v0
	v_mul_f32_e32 v0, v85, v85
	v_fmac_f32_e32 v0, v17, v17
	s_nop 1
	s_waitcnt lgkmcnt(0)
	v_add_f32_dpp v0, v0, v0 quad_perm:[1,0,3,2] row_mask:0xf bank_mask:0xf
	s_nop 1
	s_waitcnt lgkmcnt(0)
	v_add_f32_dpp v0, v0, v0 quad_perm:[2,3,0,1] row_mask:0xf bank_mask:0xf
	s_nop 1
	s_waitcnt lgkmcnt(0)
	v_add_f32_dpp v0, v0, v0 row_half_mirror row_mask:0xf bank_mask:0xf
	s_nop 1
	s_waitcnt lgkmcnt(0)
	v_add_f32_dpp v0, v0, v0 row_mirror row_mask:0xf bank_mask:0xf
	ds_swizzle_b32 v1, v0 offset:swizzle(SWAP,16)
	s_and_saveexec_b64 s[4:5], s[0:1]
	s_cbranch_execz .LBB0_183
	s_waitcnt lgkmcnt(0)
	v_add_f32_e32 v0, v0, v1
	v_add_u32_e32 v1, s25, v97
	ds_write_b32 v1, v0 offset:32768
; __device__ __forceinline__ float bf16_lo(unsigned u) { return __uint_as_float(u << 16); }
; __device__ __forceinline__ float bf16_hi(unsigned u) { return __uint_as_float(u & 0xffff0000u); }
; #define SWZ_XOR(v, o) __int_as_float(__builtin_amdgcn_ds_swizzle(__float_as_int(v), ((o) << 10) | 0x1F))
; __device__ __forceinline__ float half_sum32(float v) {
;     v += SWZ_XOR(v, 16); v += SWZ_XOR(v, 8); v += SWZ_XOR(v, 4); v += SWZ_XOR(v, 2); v += SWZ_XOR(v, 1);
;     return v;
; __device__ __forceinline__ void phase_mixer(const Params& p, LAS3 char* lds, int wid) {
;     ...
;                 const bf16_t* ub = proj + (size_t)t0 * DIN + 3072 + hd * 128 + 4 * n + cp;
;                 float ya[16], yb[16];
; #pragma unroll
;                 for (int r = 0; r < 16; ++r) {
;                     const int tt = 32 * mt + (r & 3) + 8 * (r >> 2) + 4 * kh;
;                     const unsigned uu = *(const unsigned*)(ub + (size_t)tt * DIN);
;                     const float bias = p.sgu_b[hd * 128 + tt];
;                     ya[r] = gelu_f(bf16_lo(uu)) * (acc0[r] + bias);
;                     yb[r] = gelu_f(bf16_hi(uu)) * (acc1[r] + bias);
;                     const float ps = half_sum32(ya[r] * ya[r] + yb[r] * yb[r]);
;                     if (n == 0) stat[tt * 2 + (wid & 1)] = ps;
;                 }
.LBB0_183:
	s_or_b64 exec, exec, s[4:5]
	s_waitcnt lgkmcnt(0)
	v_lshl_add_u64 v[0:1], v[80:81], 0, v[44:45]
	global_load_dword v86, v[82:83], off offset:8
	s_nop 0
	s_waitcnt vmcnt(0)
	v_mov_b32_e32 v0, v202
	v_add_f32_e32 v1, v18, v86
	v_add_f32_e32 v18, v2, v86
	s_waitcnt vmcnt(0)
	v_lshlrev_b32_e32 v2, 16, v0
	v_and_b32_e32 v0, 0xffff0000, v0
	v_fma_f32 v86, |v2|, s87, 1.0
	v_fma_f32 v88, |v0|, s87, 1.0
	v_rcp_f32_e32 v86, v86
	v_rcp_f32_e32 v88, v88
	v_mul_f32_e32 v87, v2, v2
	v_mul_f32_e32 v89, v0, v0
	v_mul_f32_e32 v87, 0xbf38aa3b, v87
	v_fmamk_f32 v90, v86, 0x3f07dc22, v126
	v_mul_f32_e32 v89, 0xbf38aa3b, v89
	v_exp_f32_e32 v87, v87
	v_fmamk_f32 v91, v88, 0x3f07dc22, v126
	v_fmaak_f32 v90, v86, v90, 0x3f35f0e3
	v_exp_f32_e32 v89, v89
	v_fmaak_f32 v91, v88, v91, 0x3f35f0e3
	v_fmaak_f32 v90, v86, v90, 0xbe11a98e
	v_fmaak_f32 v91, v88, v91, 0xbe11a98e
	v_fmaak_f32 v90, v86, v90, 0x3e027906
	v_fmaak_f32 v91, v88, v91, 0x3e027906
	v_mul_f32_e32 v86, v86, v90
	v_mul_f32_e32 v88, v88, v91
	v_mul_f32_e32 v86, v87, v86
	v_mul_f32_e32 v87, v89, v88
	v_mul_f32_e32 v88, v86, v2
	v_fma_f32 v86, -v86, v2, v2
	v_cmp_gt_f32_e32 vcc, 0, v2
	v_mul_f32_e32 v89, v87, v0
	v_fma_f32 v87, -v87, v0, v0
	v_cndmask_b32_e32 v2, v86, v88, vcc
	v_cmp_gt_f32_e32 vcc, 0, v0
	v_mul_f32_e32 v2, v1, v2
	s_nop 0
	v_cndmask_b32_e32 v0, v87, v89, vcc
	v_mul_f32_e32 v18, v18, v0
	v_mul_f32_e32 v0, v18, v18
	v_fmac_f32_e32 v0, v2, v2
	s_nop 1
	s_waitcnt lgkmcnt(0)
	v_add_f32_dpp v0, v0, v0 quad_perm:[1,0,3,2] row_mask:0xf bank_mask:0xf
	s_nop 1
	s_waitcnt lgkmcnt(0)
	v_add_f32_dpp v0, v0, v0 quad_perm:[2,3,0,1] row_mask:0xf bank_mask:0xf
	s_nop 1
	s_waitcnt lgkmcnt(0)
	v_add_f32_dpp v0, v0, v0 row_half_mirror row_mask:0xf bank_mask:0xf
	s_nop 1
	s_waitcnt lgkmcnt(0)
	v_add_f32_dpp v0, v0, v0 row_mirror row_mask:0xf bank_mask:0xf
	ds_swizzle_b32 v1, v0 offset:swizzle(SWAP,16)
	s_and_saveexec_b64 s[4:5], s[0:1]
	s_cbranch_execz .LBB0_185
	s_waitcnt lgkmcnt(0)
	v_add_f32_e32 v0, v0, v1
	v_add_u32_e32 v1, s25, v99
	ds_write_b32 v1, v0 offset:32768
.LBB0_185:
	s_or_b64 exec, exec, s[4:5]
	s_waitcnt lgkmcnt(0)
	v_lshl_add_u64 v[0:1], v[80:81], 0, v[46:47]
	global_load_dword v86, v[82:83], off offset:12
	s_waitcnt vmcnt(0)
	v_add_f32_e32 v3, v3, v86
	v_add_f32_e32 v1, v19, v86
	s_waitcnt vmcnt(0)
	v_mov_b32_e32 v0, v203
	v_lshlrev_b32_e32 v19, 16, v0
	v_and_b32_e32 v0, 0xffff0000, v0
	v_fma_f32 v86, |v19|, s87, 1.0
	v_fma_f32 v88, |v0|, s87, 1.0
	v_rcp_f32_e32 v86, v86
	v_rcp_f32_e32 v88, v88
	v_mul_f32_e32 v87, v19, v19
	v_mul_f32_e32 v89, v0, v0
	v_mul_f32_e32 v87, 0xbf38aa3b, v87
	v_fmamk_f32 v90, v86, 0x3f07dc22, v126
	v_mul_f32_e32 v89, 0xbf38aa3b, v89
	v_exp_f32_e32 v87, v87
	v_fmamk_f32 v91, v88, 0x3f07dc22, v126
	v_fmaak_f32 v90, v86, v90, 0x3f35f0e3
	v_exp_f32_e32 v89, v89
	v_fmaak_f32 v91, v88, v91, 0x3f35f0e3
	v_fmaak_f32 v90, v86, v90, 0xbe11a98e
	v_fmaak_f32 v91, v88, v91, 0xbe11a98e
	v_fmaak_f32 v90, v86, v90, 0x3e027906
	v_fmaak_f32 v91, v88, v91, 0x3e027906
	v_mul_f32_e32 v86, v86, v90
	v_mul_f32_e32 v88, v88, v91
	v_mul_f32_e32 v86, v87, v86
	v_mul_f32_e32 v87, v89, v88
	v_mul_f32_e32 v88, v86, v19
	v_fma_f32 v86, -v86, v19, v19
	v_cmp_gt_f32_e32 vcc, 0, v19
	v_mul_f32_e32 v89, v87, v0
	v_fma_f32 v87, -v87, v0, v0
	v_cndmask_b32_e32 v19, v86, v88, vcc
	v_cmp_gt_f32_e32 vcc, 0, v0
	v_mul_f32_e32 v19, v1, v19
	s_nop 0
	v_cndmask_b32_e32 v0, v87, v89, vcc
	v_mul_f32_e32 v3, v3, v0
	v_mul_f32_e32 v0, v3, v3
	v_fmac_f32_e32 v0, v19, v19
	s_nop 1
	s_waitcnt lgkmcnt(0)
	v_add_f32_dpp v0, v0, v0 quad_perm:[1,0,3,2] row_mask:0xf bank_mask:0xf
	s_nop 1
	s_waitcnt lgkmcnt(0)
	v_add_f32_dpp v0, v0, v0 quad_perm:[2,3,0,1] row_mask:0xf bank_mask:0xf
	s_nop 1
	s_waitcnt lgkmcnt(0)
	v_add_f32_dpp v0, v0, v0 row_half_mirror row_mask:0xf bank_mask:0xf
	s_nop 1
	s_waitcnt lgkmcnt(0)
	v_add_f32_dpp v0, v0, v0 row_mirror row_mask:0xf bank_mask:0xf
	ds_swizzle_b32 v1, v0 offset:swizzle(SWAP,16)
	s_and_saveexec_b64 s[4:5], s[0:1]
	s_cbranch_execz .LBB0_187
	s_waitcnt lgkmcnt(0)
	v_add_f32_e32 v0, v0, v1
	v_add_u32_e32 v1, s25, v101
	ds_write_b32 v1, v0 offset:32768
.LBB0_187:
	s_or_b64 exec, exec, s[4:5]
	s_waitcnt lgkmcnt(0)
	v_lshl_add_u64 v[0:1], v[80:81], 0, v[48:49]
	global_load_dword v86, v[82:83], off offset:32
	s_waitcnt vmcnt(0)
	v_add_f32_e32 v4, v4, v86
	v_add_f32_e32 v1, v20, v86
	s_waitcnt vmcnt(0)
	v_mov_b32_e32 v0, v204
	v_lshlrev_b32_e32 v20, 16, v0
	v_and_b32_e32 v0, 0xffff0000, v0
	v_fma_f32 v86, |v20|, s87, 1.0
	v_fma_f32 v88, |v0|, s87, 1.0
	v_rcp_f32_e32 v86, v86
	v_rcp_f32_e32 v88, v88
	v_mul_f32_e32 v87, v20, v20
	v_mul_f32_e32 v89, v0, v0
	v_mul_f32_e32 v87, 0xbf38aa3b, v87
	v_fmamk_f32 v90, v86, 0x3f07dc22, v126
	v_mul_f32_e32 v89, 0xbf38aa3b, v89
	v_exp_f32_e32 v87, v87
	v_fmamk_f32 v91, v88, 0x3f07dc22, v126
	v_fmaak_f32 v90, v86, v90, 0x3f35f0e3
	v_exp_f32_e32 v89, v89
	v_fmaak_f32 v91, v88, v91, 0x3f35f0e3
	v_fmaak_f32 v90, v86, v90, 0xbe11a98e
	v_fmaak_f32 v91, v88, v91, 0xbe11a98e
	v_fmaak_f32 v90, v86, v90, 0x3e027906
	v_fmaak_f32 v91, v88, v91, 0x3e027906
	v_mul_f32_e32 v86, v86, v90
	v_mul_f32_e32 v88, v88, v91
	v_mul_f32_e32 v86, v87, v86
	v_mul_f32_e32 v87, v89, v88
	v_mul_f32_e32 v88, v86, v20
	v_fma_f32 v86, -v86, v20, v20
	v_cmp_gt_f32_e32 vcc, 0, v20
	v_mul_f32_e32 v89, v87, v0
	v_fma_f32 v87, -v87, v0, v0
	v_cndmask_b32_e32 v20, v86, v88, vcc
	v_cmp_gt_f32_e32 vcc, 0, v0
	v_mul_f32_e32 v20, v1, v20
	s_nop 0
	v_cndmask_b32_e32 v0, v87, v89, vcc
	v_mul_f32_e32 v4, v4, v0
	v_mul_f32_e32 v0, v4, v4
	v_fmac_f32_e32 v0, v20, v20
	s_nop 1
	s_waitcnt lgkmcnt(0)
	v_add_f32_dpp v0, v0, v0 quad_perm:[1,0,3,2] row_mask:0xf bank_mask:0xf
	s_nop 1
	s_waitcnt lgkmcnt(0)
	v_add_f32_dpp v0, v0, v0 quad_perm:[2,3,0,1] row_mask:0xf bank_mask:0xf
	s_nop 1
	s_waitcnt lgkmcnt(0)
	v_add_f32_dpp v0, v0, v0 row_half_mirror row_mask:0xf bank_mask:0xf
	s_nop 1
	s_waitcnt lgkmcnt(0)
	v_add_f32_dpp v0, v0, v0 row_mirror row_mask:0xf bank_mask:0xf
	ds_swizzle_b32 v1, v0 offset:swizzle(SWAP,16)
	s_and_saveexec_b64 s[4:5], s[0:1]
	s_cbranch_execz .LBB0_189
	s_waitcnt lgkmcnt(0)
	v_add_f32_e32 v0, v0, v1
	v_add_u32_e32 v1, s25, v103
	ds_write_b32 v1, v0 offset:32768
; __device__ __forceinline__ float bf16_lo(unsigned u) { return __uint_as_float(u << 16); }
; __device__ __forceinline__ float bf16_hi(unsigned u) { return __uint_as_float(u & 0xffff0000u); }
; #define SWZ_XOR(v, o) __int_as_float(__builtin_amdgcn_ds_swizzle(__float_as_int(v), ((o) << 10) | 0x1F))
; __device__ __forceinline__ float half_sum32(float v) {
;     v += SWZ_XOR(v, 16); v += SWZ_XOR(v, 8); v += SWZ_XOR(v, 4); v += SWZ_XOR(v, 2); v += SWZ_XOR(v, 1);
;     return v;
; __device__ __forceinline__ void phase_mixer(const Params& p, LAS3 char* lds, int wid) {
;     ...
;                 const bf16_t* ub = proj + (size_t)t0 * DIN + 3072 + hd * 128 + 4 * n + cp;
;                 float ya[16], yb[16];
; #pragma unroll
;                 for (int r = 0; r < 16; ++r) {
;                     const int tt = 32 * mt + (r & 3) + 8 * (r >> 2) + 4 * kh;
;                     const unsigned uu = *(const unsigned*)(ub + (size_t)tt * DIN);
;                     const float bias = p.sgu_b[hd * 128 + tt];
;                     ya[r] = gelu_f(bf16_lo(uu)) * (acc0[r] + bias);
;                     yb[r] = gelu_f(bf16_hi(uu)) * (acc1[r] + bias);
;                     const float ps = half_sum32(ya[r] * ya[r] + yb[r] * yb[r]);
;                     if (n == 0) stat[tt * 2 + (wid & 1)] = ps;
;                 }
.LBB0_189:
	s_or_b64 exec, exec, s[4:5]
	s_waitcnt lgkmcnt(0)
	v_lshl_add_u64 v[0:1], v[80:81], 0, v[50:51]
	global_load_dword v86, v[82:83], off offset:36
	s_waitcnt vmcnt(0)
	v_add_f32_e32 v5, v5, v86
	v_add_f32_e32 v1, v21, v86
	s_waitcnt vmcnt(0)
	v_mov_b32_e32 v0, v205
	v_lshlrev_b32_e32 v21, 16, v0
	v_and_b32_e32 v0, 0xffff0000, v0
	v_fma_f32 v86, |v21|, s87, 1.0
	v_fma_f32 v88, |v0|, s87, 1.0
	v_rcp_f32_e32 v86, v86
	v_rcp_f32_e32 v88, v88
	v_mul_f32_e32 v87, v21, v21
	v_mul_f32_e32 v89, v0, v0
	v_mul_f32_e32 v87, 0xbf38aa3b, v87
	v_fmamk_f32 v90, v86, 0x3f07dc22, v126
	v_mul_f32_e32 v89, 0xbf38aa3b, v89
	v_exp_f32_e32 v87, v87
	v_fmamk_f32 v91, v88, 0x3f07dc22, v126
	v_fmaak_f32 v90, v86, v90, 0x3f35f0e3
	v_exp_f32_e32 v89, v89
	v_fmaak_f32 v91, v88, v91, 0x3f35f0e3
	v_fmaak_f32 v90, v86, v90, 0xbe11a98e
	v_fmaak_f32 v91, v88, v91, 0xbe11a98e
	v_fmaak_f32 v90, v86, v90, 0x3e027906
	v_fmaak_f32 v91, v88, v91, 0x3e027906
	v_mul_f32_e32 v86, v86, v90
	v_mul_f32_e32 v88, v88, v91
	v_mul_f32_e32 v86, v87, v86
	v_mul_f32_e32 v87, v89, v88
	v_mul_f32_e32 v88, v86, v21
	v_fma_f32 v86, -v86, v21, v21
	v_cmp_gt_f32_e32 vcc, 0, v21
	v_mul_f32_e32 v89, v87, v0
	v_fma_f32 v87, -v87, v0, v0
	v_cndmask_b32_e32 v21, v86, v88, vcc
	v_cmp_gt_f32_e32 vcc, 0, v0
	v_mul_f32_e32 v21, v1, v21
	s_nop 0
	v_cndmask_b32_e32 v0, v87, v89, vcc
	v_mul_f32_e32 v5, v5, v0
	v_mul_f32_e32 v0, v5, v5
	v_fmac_f32_e32 v0, v21, v21
	s_nop 1
	s_waitcnt lgkmcnt(0)
	v_add_f32_dpp v0, v0, v0 quad_perm:[1,0,3,2] row_mask:0xf bank_mask:0xf
	s_nop 1
	s_waitcnt lgkmcnt(0)
	v_add_f32_dpp v0, v0, v0 quad_perm:[2,3,0,1] row_mask:0xf bank_mask:0xf
	s_nop 1
	s_waitcnt lgkmcnt(0)
	v_add_f32_dpp v0, v0, v0 row_half_mirror row_mask:0xf bank_mask:0xf
	s_nop 1
	s_waitcnt lgkmcnt(0)
	v_add_f32_dpp v0, v0, v0 row_mirror row_mask:0xf bank_mask:0xf
	ds_swizzle_b32 v1, v0 offset:swizzle(SWAP,16)
	s_and_saveexec_b64 s[4:5], s[0:1]
	s_cbranch_execz .LBB0_191
	s_waitcnt lgkmcnt(0)
	v_add_f32_e32 v0, v0, v1
	v_add_u32_e32 v1, s25, v105
	ds_write_b32 v1, v0 offset:32768
.LBB0_191:
	s_or_b64 exec, exec, s[4:5]
	s_waitcnt lgkmcnt(0)
	v_lshl_add_u64 v[0:1], v[80:81], 0, v[52:53]
	global_load_dword v86, v[82:83], off offset:40
	s_waitcnt vmcnt(0)
	v_add_f32_e32 v6, v6, v86
	v_add_f32_e32 v1, v22, v86
	s_waitcnt vmcnt(0)
	v_mov_b32_e32 v0, v206
	v_lshlrev_b32_e32 v22, 16, v0
	v_and_b32_e32 v0, 0xffff0000, v0
	v_fma_f32 v86, |v22|, s87, 1.0
	v_fma_f32 v88, |v0|, s87, 1.0
	v_rcp_f32_e32 v86, v86
	v_rcp_f32_e32 v88, v88
	v_mul_f32_e32 v87, v22, v22
	v_mul_f32_e32 v89, v0, v0
	v_mul_f32_e32 v87, 0xbf38aa3b, v87
	v_fmamk_f32 v90, v86, 0x3f07dc22, v126
	v_mul_f32_e32 v89, 0xbf38aa3b, v89
	v_exp_f32_e32 v87, v87
	v_fmamk_f32 v91, v88, 0x3f07dc22, v126
	v_fmaak_f32 v90, v86, v90, 0x3f35f0e3
	v_exp_f32_e32 v89, v89
	v_fmaak_f32 v91, v88, v91, 0x3f35f0e3
	v_fmaak_f32 v90, v86, v90, 0xbe11a98e
	v_fmaak_f32 v91, v88, v91, 0xbe11a98e
	v_fmaak_f32 v90, v86, v90, 0x3e027906
	v_fmaak_f32 v91, v88, v91, 0x3e027906
	v_mul_f32_e32 v86, v86, v90
	v_mul_f32_e32 v88, v88, v91
	v_mul_f32_e32 v86, v87, v86
	v_mul_f32_e32 v87, v89, v88
	v_mul_f32_e32 v88, v86, v22
	v_fma_f32 v86, -v86, v22, v22
	v_cmp_gt_f32_e32 vcc, 0, v22
	v_mul_f32_e32 v89, v87, v0
	v_fma_f32 v87, -v87, v0, v0
	v_cndmask_b32_e32 v22, v86, v88, vcc
	v_cmp_gt_f32_e32 vcc, 0, v0
	v_mul_f32_e32 v22, v1, v22
	s_nop 0
	v_cndmask_b32_e32 v0, v87, v89, vcc
	v_mul_f32_e32 v6, v6, v0
	v_mul_f32_e32 v0, v6, v6
	v_fmac_f32_e32 v0, v22, v22
	s_nop 1
	s_waitcnt lgkmcnt(0)
	v_add_f32_dpp v0, v0, v0 quad_perm:[1,0,3,2] row_mask:0xf bank_mask:0xf
	s_nop 1
	s_waitcnt lgkmcnt(0)
	v_add_f32_dpp v0, v0, v0 quad_perm:[2,3,0,1] row_mask:0xf bank_mask:0xf
	s_nop 1
	s_waitcnt lgkmcnt(0)
	v_add_f32_dpp v0, v0, v0 row_half_mirror row_mask:0xf bank_mask:0xf
	s_nop 1
	s_waitcnt lgkmcnt(0)
	v_add_f32_dpp v0, v0, v0 row_mirror row_mask:0xf bank_mask:0xf
	ds_swizzle_b32 v1, v0 offset:swizzle(SWAP,16)
	s_and_saveexec_b64 s[4:5], s[0:1]
	s_cbranch_execz .LBB0_193
	s_waitcnt lgkmcnt(0)
	v_add_f32_e32 v0, v0, v1
	v_add_u32_e32 v1, s25, v107
	ds_write_b32 v1, v0 offset:32768
.LBB0_193:
	s_or_b64 exec, exec, s[4:5]
	s_waitcnt lgkmcnt(0)
	v_lshl_add_u64 v[0:1], v[80:81], 0, v[54:55]
	global_load_dword v82, v[82:83], off offset:44
	s_waitcnt vmcnt(0)
	v_add_f32_e32 v7, v7, v82
	v_add_f32_e32 v1, v23, v82
	s_waitcnt vmcnt(0)
	v_mov_b32_e32 v0, v207
	v_lshlrev_b32_e32 v23, 16, v0
	v_and_b32_e32 v0, 0xffff0000, v0
	v_fma_f32 v82, |v23|, s87, 1.0
	v_fma_f32 v86, |v0|, s87, 1.0
	v_rcp_f32_e32 v82, v82
	v_rcp_f32_e32 v86, v86
	v_mul_f32_e32 v83, v23, v23
	v_mul_f32_e32 v87, v0, v0
	v_mul_f32_e32 v83, 0xbf38aa3b, v83
	v_fmamk_f32 v88, v82, 0x3f07dc22, v126
	v_mul_f32_e32 v87, 0xbf38aa3b, v87
	v_exp_f32_e32 v83, v83
	v_fmamk_f32 v89, v86, 0x3f07dc22, v126
	v_fmaak_f32 v88, v82, v88, 0x3f35f0e3
	v_exp_f32_e32 v87, v87
	v_fmaak_f32 v89, v86, v89, 0x3f35f0e3
	v_fmaak_f32 v88, v82, v88, 0xbe11a98e
	v_fmaak_f32 v89, v86, v89, 0xbe11a98e
	v_fmaak_f32 v88, v82, v88, 0x3e027906
	v_fmaak_f32 v89, v86, v89, 0x3e027906
	v_mul_f32_e32 v82, v82, v88
	v_mul_f32_e32 v86, v86, v89
	v_mul_f32_e32 v82, v83, v82
	v_mul_f32_e32 v83, v87, v86
	v_mul_f32_e32 v86, v82, v23
	v_fma_f32 v82, -v82, v23, v23
	v_cmp_gt_f32_e32 vcc, 0, v23
	v_mul_f32_e32 v87, v83, v0
	v_fma_f32 v83, -v83, v0, v0
	v_cndmask_b32_e32 v23, v82, v86, vcc
	v_cmp_gt_f32_e32 vcc, 0, v0
	v_mul_f32_e32 v23, v1, v23
	s_nop 0
	v_cndmask_b32_e32 v0, v83, v87, vcc
	v_mul_f32_e32 v7, v7, v0
	v_mul_f32_e32 v0, v7, v7
	v_fmac_f32_e32 v0, v23, v23
	s_nop 1
	s_waitcnt lgkmcnt(0)
	v_add_f32_dpp v0, v0, v0 quad_perm:[1,0,3,2] row_mask:0xf bank_mask:0xf
	s_nop 1
	s_waitcnt lgkmcnt(0)
	v_add_f32_dpp v0, v0, v0 quad_perm:[2,3,0,1] row_mask:0xf bank_mask:0xf
	s_nop 1
	s_waitcnt lgkmcnt(0)
	v_add_f32_dpp v0, v0, v0 row_half_mirror row_mask:0xf bank_mask:0xf
	s_nop 1
	s_waitcnt lgkmcnt(0)
	v_add_f32_dpp v0, v0, v0 row_mirror row_mask:0xf bank_mask:0xf
	ds_swizzle_b32 v1, v0 offset:swizzle(SWAP,16)
	s_and_saveexec_b64 s[4:5], s[0:1]
	s_cbranch_execz .LBB0_195
	s_waitcnt lgkmcnt(0)
	v_add_f32_e32 v0, v0, v1
	v_add_u32_e32 v1, s25, v109
	ds_write_b32 v1, v0 offset:32768
; __device__ __forceinline__ float bf16_lo(unsigned u) { return __uint_as_float(u << 16); }
; __device__ __forceinline__ float bf16_hi(unsigned u) { return __uint_as_float(u & 0xffff0000u); }
; #define SWZ_XOR(v, o) __int_as_float(__builtin_amdgcn_ds_swizzle(__float_as_int(v), ((o) << 10) | 0x1F))
; __device__ __forceinline__ float half_sum32(float v) {
;     v += SWZ_XOR(v, 16); v += SWZ_XOR(v, 8); v += SWZ_XOR(v, 4); v += SWZ_XOR(v, 2); v += SWZ_XOR(v, 1);
;     return v;
; __device__ __forceinline__ void phase_mixer(const Params& p, LAS3 char* lds, int wid) {
;     ...
;                 const bf16_t* ub = proj + (size_t)t0 * DIN + 3072 + hd * 128 + 4 * n + cp;
;                 float ya[16], yb[16];
; #pragma unroll
;                 for (int r = 0; r < 16; ++r) {
;                     const int tt = 32 * mt + (r & 3) + 8 * (r >> 2) + 4 * kh;
;                     const unsigned uu = *(const unsigned*)(ub + (size_t)tt * DIN);
;                     const float bias = p.sgu_b[hd * 128 + tt];
;                     ya[r] = gelu_f(bf16_lo(uu)) * (acc0[r] + bias);
;                     yb[r] = gelu_f(bf16_hi(uu)) * (acc1[r] + bias);
;                     const float ps = half_sum32(ya[r] * ya[r] + yb[r] * yb[r]);
;                     if (n == 0) stat[tt * 2 + (wid & 1)] = ps;
;                 }
.LBB0_195:
	s_or_b64 exec, exec, s[4:5]
	s_waitcnt lgkmcnt(0)
	v_lshl_add_u64 v[0:1], v[80:81], 0, v[56:57]
	v_add_u32_e32 v0, s92, v110
	v_ashrrev_i32_e32 v1, 31, v0
	v_lshl_add_u64 v[0:1], v[0:1], 2, s[98:99]
	global_load_dword v0, v[0:1], off
	s_waitcnt vmcnt(0)
	v_mov_b32_e32 v82, v208
	v_lshlrev_b32_e32 v1, 16, v82
	v_and_b32_e32 v82, 0xffff0000, v82
	v_fma_f32 v83, |v1|, s87, 1.0
	v_fma_f32 v87, |v82|, s87, 1.0
	v_rcp_f32_e32 v83, v83
	v_rcp_f32_e32 v87, v87
	v_mul_f32_e32 v86, v1, v1
	v_mul_f32_e32 v88, v82, v82
	v_mul_f32_e32 v86, 0xbf38aa3b, v86
	v_mul_f32_e32 v88, 0xbf38aa3b, v88
	s_waitcnt vmcnt(0)
	v_add_f32_e32 v24, v24, v0
	v_add_f32_e32 v0, v8, v0
	v_exp_f32_e32 v8, v86
	v_exp_f32_e32 v86, v88
	v_fmamk_f32 v88, v83, 0x3f07dc22, v126
	v_fmamk_f32 v89, v87, 0x3f07dc22, v126
	v_fmaak_f32 v88, v83, v88, 0x3f35f0e3
	v_fmaak_f32 v89, v87, v89, 0x3f35f0e3
	v_fmaak_f32 v88, v83, v88, 0xbe11a98e
	v_fmaak_f32 v89, v87, v89, 0xbe11a98e
	v_fmaak_f32 v88, v83, v88, 0x3e027906
	v_fmaak_f32 v89, v87, v89, 0x3e027906
	v_mul_f32_e32 v83, v83, v88
	v_mul_f32_e32 v87, v87, v89
	v_mul_f32_e32 v8, v8, v83
	v_mul_f32_e32 v83, v86, v87
	v_mul_f32_e32 v86, v8, v1
	v_fma_f32 v8, -v8, v1, v1
	v_cmp_gt_f32_e32 vcc, 0, v1
	v_mul_f32_e32 v87, v83, v82
	v_fma_f32 v83, -v83, v82, v82
	v_cndmask_b32_e32 v1, v8, v86, vcc
	v_cmp_gt_f32_e32 vcc, 0, v82
	v_mul_f32_e32 v24, v24, v1
	s_nop 0
	v_cndmask_b32_e32 v8, v83, v87, vcc
	v_mul_f32_e32 v8, v0, v8
	v_mul_f32_e32 v0, v8, v8
	v_fmac_f32_e32 v0, v24, v24
	s_nop 1
	s_waitcnt lgkmcnt(0)
	v_add_f32_dpp v0, v0, v0 quad_perm:[1,0,3,2] row_mask:0xf bank_mask:0xf
	s_nop 1
	s_waitcnt lgkmcnt(0)
	v_add_f32_dpp v0, v0, v0 quad_perm:[2,3,0,1] row_mask:0xf bank_mask:0xf
	s_nop 1
	s_waitcnt lgkmcnt(0)
	v_add_f32_dpp v0, v0, v0 row_half_mirror row_mask:0xf bank_mask:0xf
	s_nop 1
	s_waitcnt lgkmcnt(0)
	v_add_f32_dpp v0, v0, v0 row_mirror row_mask:0xf bank_mask:0xf
	ds_swizzle_b32 v1, v0 offset:swizzle(SWAP,16)
	s_and_saveexec_b64 s[4:5], s[0:1]
	s_cbranch_execz .LBB0_197
	s_waitcnt lgkmcnt(0)
	v_add_f32_e32 v0, v0, v1
	v_add_u32_e32 v1, s25, v111
	ds_write_b32 v1, v0 offset:32768
.LBB0_197:
	s_or_b64 exec, exec, s[4:5]
	s_waitcnt lgkmcnt(0)
	v_lshl_add_u64 v[0:1], v[80:81], 0, v[62:63]
	v_add_u32_e32 v0, s92, v112
	v_ashrrev_i32_e32 v1, 31, v0
	v_lshl_add_u64 v[0:1], v[0:1], 2, s[98:99]
	global_load_dword v0, v[0:1], off
	s_waitcnt vmcnt(0)
	v_mov_b32_e32 v82, v209
	v_lshlrev_b32_e32 v1, 16, v82
	v_and_b32_e32 v82, 0xffff0000, v82
	v_fma_f32 v83, |v1|, s87, 1.0
	v_fma_f32 v87, |v82|, s87, 1.0
	v_rcp_f32_e32 v83, v83
	v_rcp_f32_e32 v87, v87
	v_mul_f32_e32 v86, v1, v1
	v_mul_f32_e32 v88, v82, v82
	v_mul_f32_e32 v86, 0xbf38aa3b, v86
	v_mul_f32_e32 v88, 0xbf38aa3b, v88
	s_waitcnt vmcnt(0)
	v_add_f32_e32 v25, v25, v0
	v_add_f32_e32 v0, v9, v0
	v_exp_f32_e32 v9, v86
	v_exp_f32_e32 v86, v88
	v_fmamk_f32 v88, v83, 0x3f07dc22, v126
	v_fmamk_f32 v89, v87, 0x3f07dc22, v126
	v_fmaak_f32 v88, v83, v88, 0x3f35f0e3
	v_fmaak_f32 v89, v87, v89, 0x3f35f0e3
	v_fmaak_f32 v88, v83, v88, 0xbe11a98e
	v_fmaak_f32 v89, v87, v89, 0xbe11a98e
	v_fmaak_f32 v88, v83, v88, 0x3e027906
	v_fmaak_f32 v89, v87, v89, 0x3e027906
	v_mul_f32_e32 v83, v83, v88
	v_mul_f32_e32 v87, v87, v89
	v_mul_f32_e32 v9, v9, v83
	v_mul_f32_e32 v83, v86, v87
	v_mul_f32_e32 v86, v9, v1
	v_fma_f32 v9, -v9, v1, v1
	v_cmp_gt_f32_e32 vcc, 0, v1
	v_mul_f32_e32 v87, v83, v82
	v_fma_f32 v83, -v83, v82, v82
	v_cndmask_b32_e32 v1, v9, v86, vcc
	v_cmp_gt_f32_e32 vcc, 0, v82
	v_mul_f32_e32 v25, v25, v1
	s_nop 0
	v_cndmask_b32_e32 v9, v83, v87, vcc
	v_mul_f32_e32 v9, v0, v9
	v_mul_f32_e32 v0, v9, v9
	v_fmac_f32_e32 v0, v25, v25
	s_nop 1
	s_waitcnt lgkmcnt(0)
	v_add_f32_dpp v0, v0, v0 quad_perm:[1,0,3,2] row_mask:0xf bank_mask:0xf
	s_nop 1
	s_waitcnt lgkmcnt(0)
	v_add_f32_dpp v0, v0, v0 quad_perm:[2,3,0,1] row_mask:0xf bank_mask:0xf
	s_nop 1
	s_waitcnt lgkmcnt(0)
	v_add_f32_dpp v0, v0, v0 row_half_mirror row_mask:0xf bank_mask:0xf
	s_nop 1
	s_waitcnt lgkmcnt(0)
	v_add_f32_dpp v0, v0, v0 row_mirror row_mask:0xf bank_mask:0xf
	ds_swizzle_b32 v1, v0 offset:swizzle(SWAP,16)
	s_and_saveexec_b64 s[4:5], s[0:1]
	s_cbranch_execz .LBB0_199
	s_waitcnt lgkmcnt(0)
	v_add_f32_e32 v0, v0, v1
	v_add_u32_e32 v1, s25, v113
	ds_write_b32 v1, v0 offset:32768
.LBB0_199:
	s_or_b64 exec, exec, s[4:5]
	s_waitcnt lgkmcnt(0)
	v_lshl_add_u64 v[0:1], v[80:81], 0, v[64:65]
	v_add_u32_e32 v0, s92, v114
	v_ashrrev_i32_e32 v1, 31, v0
	v_lshl_add_u64 v[0:1], v[0:1], 2, s[98:99]
	global_load_dword v0, v[0:1], off
	s_waitcnt vmcnt(0)
	v_mov_b32_e32 v82, v210
	v_lshlrev_b32_e32 v1, 16, v82
	v_and_b32_e32 v82, 0xffff0000, v82
	v_fma_f32 v83, |v1|, s87, 1.0
	v_fma_f32 v87, |v82|, s87, 1.0
	v_rcp_f32_e32 v83, v83
	v_rcp_f32_e32 v87, v87
	v_mul_f32_e32 v86, v1, v1
	v_mul_f32_e32 v88, v82, v82
	v_mul_f32_e32 v86, 0xbf38aa3b, v86
	v_mul_f32_e32 v88, 0xbf38aa3b, v88
	s_waitcnt vmcnt(0)
	v_add_f32_e32 v26, v26, v0
	v_add_f32_e32 v0, v10, v0
	v_exp_f32_e32 v10, v86
	v_exp_f32_e32 v86, v88
	v_fmamk_f32 v88, v83, 0x3f07dc22, v126
	v_fmamk_f32 v89, v87, 0x3f07dc22, v126
	v_fmaak_f32 v88, v83, v88, 0x3f35f0e3
	v_fmaak_f32 v89, v87, v89, 0x3f35f0e3
	v_fmaak_f32 v88, v83, v88, 0xbe11a98e
	v_fmaak_f32 v89, v87, v89, 0xbe11a98e
	v_fmaak_f32 v88, v83, v88, 0x3e027906
	v_fmaak_f32 v89, v87, v89, 0x3e027906
	v_mul_f32_e32 v83, v83, v88
	v_mul_f32_e32 v87, v87, v89
	v_mul_f32_e32 v10, v10, v83
	v_mul_f32_e32 v83, v86, v87
	v_mul_f32_e32 v86, v10, v1
	v_fma_f32 v10, -v10, v1, v1
	v_cmp_gt_f32_e32 vcc, 0, v1
	v_mul_f32_e32 v87, v83, v82
	v_fma_f32 v83, -v83, v82, v82
	v_cndmask_b32_e32 v1, v10, v86, vcc
	v_cmp_gt_f32_e32 vcc, 0, v82
	v_mul_f32_e32 v26, v26, v1
	s_nop 0
	v_cndmask_b32_e32 v10, v83, v87, vcc
	v_mul_f32_e32 v10, v0, v10
	v_mul_f32_e32 v0, v10, v10
	v_fmac_f32_e32 v0, v26, v26
	s_nop 1
	s_waitcnt lgkmcnt(0)
	v_add_f32_dpp v0, v0, v0 quad_perm:[1,0,3,2] row_mask:0xf bank_mask:0xf
	s_nop 1
	s_waitcnt lgkmcnt(0)
	v_add_f32_dpp v0, v0, v0 quad_perm:[2,3,0,1] row_mask:0xf bank_mask:0xf
	s_nop 1
	s_waitcnt lgkmcnt(0)
	v_add_f32_dpp v0, v0, v0 row_half_mirror row_mask:0xf bank_mask:0xf
	s_nop 1
	s_waitcnt lgkmcnt(0)
	v_add_f32_dpp v0, v0, v0 row_mirror row_mask:0xf bank_mask:0xf
	ds_swizzle_b32 v1, v0 offset:swizzle(SWAP,16)
	s_and_saveexec_b64 s[4:5], s[0:1]
	s_cbranch_execz .LBB0_201
	s_waitcnt lgkmcnt(0)
	v_add_f32_e32 v0, v0, v1
	v_add_u32_e32 v1, s25, v115
	ds_write_b32 v1, v0 offset:32768
; __device__ __forceinline__ float bf16_lo(unsigned u) { return __uint_as_float(u << 16); }
; __device__ __forceinline__ float bf16_hi(unsigned u) { return __uint_as_float(u & 0xffff0000u); }
; #define SWZ_XOR(v, o) __int_as_float(__builtin_amdgcn_ds_swizzle(__float_as_int(v), ((o) << 10) | 0x1F))
; __device__ __forceinline__ float half_sum32(float v) {
;     v += SWZ_XOR(v, 16); v += SWZ_XOR(v, 8); v += SWZ_XOR(v, 4); v += SWZ_XOR(v, 2); v += SWZ_XOR(v, 1);
;     return v;
; __device__ __forceinline__ void phase_mixer(const Params& p, LAS3 char* lds, int wid) {
;     ...
;                 const bf16_t* ub = proj + (size_t)t0 * DIN + 3072 + hd * 128 + 4 * n + cp;
;                 float ya[16], yb[16];
; #pragma unroll
;                 for (int r = 0; r < 16; ++r) {
;                     const int tt = 32 * mt + (r & 3) + 8 * (r >> 2) + 4 * kh;
;                     const unsigned uu = *(const unsigned*)(ub + (size_t)tt * DIN);
;                     const float bias = p.sgu_b[hd * 128 + tt];
;                     ya[r] = gelu_f(bf16_lo(uu)) * (acc0[r] + bias);
;                     yb[r] = gelu_f(bf16_hi(uu)) * (acc1[r] + bias);
;                     const float ps = half_sum32(ya[r] * ya[r] + yb[r] * yb[r]);
;                     if (n == 0) stat[tt * 2 + (wid & 1)] = ps;
.LBB0_201:
	s_or_b64 exec, exec, s[4:5]
	s_waitcnt lgkmcnt(0)
	v_lshl_add_u64 v[0:1], v[80:81], 0, v[66:67]
	v_add_u32_e32 v0, s92, v116
	v_ashrrev_i32_e32 v1, 31, v0
	v_lshl_add_u64 v[0:1], v[0:1], 2, s[98:99]
	global_load_dword v0, v[0:1], off
	s_waitcnt vmcnt(0)
	v_mov_b32_e32 v82, v211
	v_lshlrev_b32_e32 v1, 16, v82
	v_and_b32_e32 v82, 0xffff0000, v82
	v_fma_f32 v83, |v1|, s87, 1.0
	v_fma_f32 v87, |v82|, s87, 1.0
	v_rcp_f32_e32 v83, v83
	v_rcp_f32_e32 v87, v87
	v_mul_f32_e32 v86, v1, v1
	v_mul_f32_e32 v88, v82, v82
	v_mul_f32_e32 v86, 0xbf38aa3b, v86
	v_mul_f32_e32 v88, 0xbf38aa3b, v88
	s_waitcnt vmcnt(0)
	v_add_f32_e32 v27, v27, v0
	v_add_f32_e32 v0, v11, v0
	v_exp_f32_e32 v11, v86
	v_exp_f32_e32 v86, v88
	v_fmamk_f32 v88, v83, 0x3f07dc22, v126
	v_fmamk_f32 v89, v87, 0x3f07dc22, v126
	v_fmaak_f32 v88, v83, v88, 0x3f35f0e3
	v_fmaak_f32 v89, v87, v89, 0x3f35f0e3
	v_fmaak_f32 v88, v83, v88, 0xbe11a98e
	v_fmaak_f32 v89, v87, v89, 0xbe11a98e
	v_fmaak_f32 v88, v83, v88, 0x3e027906
	v_fmaak_f32 v89, v87, v89, 0x3e027906
	v_mul_f32_e32 v83, v83, v88
	v_mul_f32_e32 v87, v87, v89
	v_mul_f32_e32 v11, v11, v83
	v_mul_f32_e32 v83, v86, v87
	v_mul_f32_e32 v86, v11, v1
	v_fma_f32 v11, -v11, v1, v1
	v_cmp_gt_f32_e32 vcc, 0, v1
	v_mul_f32_e32 v87, v83, v82
	v_fma_f32 v83, -v83, v82, v82
	v_cndmask_b32_e32 v1, v11, v86, vcc
	v_cmp_gt_f32_e32 vcc, 0, v82
	v_mul_f32_e32 v27, v27, v1
	s_nop 0
	v_cndmask_b32_e32 v11, v83, v87, vcc
	v_mul_f32_e32 v11, v0, v11
	v_mul_f32_e32 v0, v11, v11
	v_fmac_f32_e32 v0, v27, v27
	s_nop 1
	s_waitcnt lgkmcnt(0)
	v_add_f32_dpp v0, v0, v0 quad_perm:[1,0,3,2] row_mask:0xf bank_mask:0xf
	s_nop 1
	s_waitcnt lgkmcnt(0)
	v_add_f32_dpp v0, v0, v0 quad_perm:[2,3,0,1] row_mask:0xf bank_mask:0xf
	s_nop 1
	s_waitcnt lgkmcnt(0)
	v_add_f32_dpp v0, v0, v0 row_half_mirror row_mask:0xf bank_mask:0xf
	s_nop 1
	s_waitcnt lgkmcnt(0)
	v_add_f32_dpp v0, v0, v0 row_mirror row_mask:0xf bank_mask:0xf
	ds_swizzle_b32 v1, v0 offset:swizzle(SWAP,16)
	s_and_saveexec_b64 s[4:5], s[0:1]
	s_cbranch_execz .LBB0_203
	s_waitcnt lgkmcnt(0)
	v_add_f32_e32 v0, v0, v1
	v_add_u32_e32 v1, s25, v117
	ds_write_b32 v1, v0 offset:32768
.LBB0_203:
	s_or_b64 exec, exec, s[4:5]
	s_waitcnt lgkmcnt(0)
	v_lshl_add_u64 v[0:1], v[80:81], 0, v[68:69]
	v_add_u32_e32 v0, s92, v118
	v_ashrrev_i32_e32 v1, 31, v0
	v_lshl_add_u64 v[0:1], v[0:1], 2, s[98:99]
	global_load_dword v0, v[0:1], off
	s_waitcnt vmcnt(0)
	v_mov_b32_e32 v82, v212
	v_lshlrev_b32_e32 v1, 16, v82
	v_and_b32_e32 v82, 0xffff0000, v82
	v_fma_f32 v83, |v1|, s87, 1.0
	v_fma_f32 v87, |v82|, s87, 1.0
	v_rcp_f32_e32 v83, v83
	v_rcp_f32_e32 v87, v87
	v_mul_f32_e32 v86, v1, v1
	v_mul_f32_e32 v88, v82, v82
	v_mul_f32_e32 v86, 0xbf38aa3b, v86
	v_mul_f32_e32 v88, 0xbf38aa3b, v88
	s_waitcnt vmcnt(0)
	v_add_f32_e32 v28, v28, v0
	v_add_f32_e32 v0, v12, v0
	v_exp_f32_e32 v12, v86
	v_exp_f32_e32 v86, v88
	v_fmamk_f32 v88, v83, 0x3f07dc22, v126
	v_fmamk_f32 v89, v87, 0x3f07dc22, v126
	v_fmaak_f32 v88, v83, v88, 0x3f35f0e3
	v_fmaak_f32 v89, v87, v89, 0x3f35f0e3
	v_fmaak_f32 v88, v83, v88, 0xbe11a98e
	v_fmaak_f32 v89, v87, v89, 0xbe11a98e
	v_fmaak_f32 v88, v83, v88, 0x3e027906
	v_fmaak_f32 v89, v87, v89, 0x3e027906
	v_mul_f32_e32 v83, v83, v88
	v_mul_f32_e32 v87, v87, v89
	v_mul_f32_e32 v12, v12, v83
	v_mul_f32_e32 v83, v86, v87
	v_mul_f32_e32 v86, v12, v1
	v_fma_f32 v12, -v12, v1, v1
	v_cmp_gt_f32_e32 vcc, 0, v1
	v_mul_f32_e32 v87, v83, v82
	v_fma_f32 v83, -v83, v82, v82
	v_cndmask_b32_e32 v1, v12, v86, vcc
	v_cmp_gt_f32_e32 vcc, 0, v82
	v_mul_f32_e32 v28, v28, v1
	s_nop 0
	v_cndmask_b32_e32 v12, v83, v87, vcc
	v_mul_f32_e32 v12, v0, v12
	v_mul_f32_e32 v0, v12, v12
	v_fmac_f32_e32 v0, v28, v28
	s_nop 1
	s_waitcnt lgkmcnt(0)
	v_add_f32_dpp v0, v0, v0 quad_perm:[1,0,3,2] row_mask:0xf bank_mask:0xf
	s_nop 1
	s_waitcnt lgkmcnt(0)
	v_add_f32_dpp v0, v0, v0 quad_perm:[2,3,0,1] row_mask:0xf bank_mask:0xf
	s_nop 1
	s_waitcnt lgkmcnt(0)
	v_add_f32_dpp v0, v0, v0 row_half_mirror row_mask:0xf bank_mask:0xf
	s_nop 1
	s_waitcnt lgkmcnt(0)
	v_add_f32_dpp v0, v0, v0 row_mirror row_mask:0xf bank_mask:0xf
	ds_swizzle_b32 v1, v0 offset:swizzle(SWAP,16)
	s_and_saveexec_b64 s[4:5], s[0:1]
	s_cbranch_execz .LBB0_205
	s_waitcnt lgkmcnt(0)
	v_add_f32_e32 v0, v0, v1
	v_add_u32_e32 v1, s25, v119
	ds_write_b32 v1, v0 offset:32768
; __device__ __forceinline__ float bf16_lo(unsigned u) { return __uint_as_float(u << 16); }
; __device__ __forceinline__ float bf16_hi(unsigned u) { return __uint_as_float(u & 0xffff0000u); }
; #define SWZ_XOR(v, o) __int_as_float(__builtin_amdgcn_ds_swizzle(__float_as_int(v), ((o) << 10) | 0x1F))
; __device__ __forceinline__ float half_sum32(float v) {
;     v += SWZ_XOR(v, 16); v += SWZ_XOR(v, 8); v += SWZ_XOR(v, 4); v += SWZ_XOR(v, 2); v += SWZ_XOR(v, 1);
;     return v;
; __device__ __forceinline__ void phase_mixer(const Params& p, LAS3 char* lds, int wid) {
;     ...
;                 const bf16_t* ub = proj + (size_t)t0 * DIN + 3072 + hd * 128 + 4 * n + cp;
;                 float ya[16], yb[16];
; #pragma unroll
;                 for (int r = 0; r < 16; ++r) {
;                     const int tt = 32 * mt + (r & 3) + 8 * (r >> 2) + 4 * kh;
;                     const unsigned uu = *(const unsigned*)(ub + (size_t)tt * DIN);
;                     const float bias = p.sgu_b[hd * 128 + tt];
;                     ya[r] = gelu_f(bf16_lo(uu)) * (acc0[r] + bias);
;                     yb[r] = gelu_f(bf16_hi(uu)) * (acc1[r] + bias);
;                     const float ps = half_sum32(ya[r] * ya[r] + yb[r] * yb[r]);
;                     if (n == 0) stat[tt * 2 + (wid & 1)] = ps;
.LBB0_205:
	s_or_b64 exec, exec, s[4:5]
	s_waitcnt lgkmcnt(0)
	v_lshl_add_u64 v[0:1], v[80:81], 0, v[70:71]
	v_add_u32_e32 v0, s92, v120
	v_ashrrev_i32_e32 v1, 31, v0
	v_lshl_add_u64 v[0:1], v[0:1], 2, s[98:99]
	global_load_dword v0, v[0:1], off
	s_waitcnt vmcnt(0)
	v_mov_b32_e32 v82, v213
	v_lshlrev_b32_e32 v1, 16, v82
	v_and_b32_e32 v82, 0xffff0000, v82
	v_fma_f32 v83, |v1|, s87, 1.0
	v_fma_f32 v87, |v82|, s87, 1.0
	v_rcp_f32_e32 v83, v83
	v_rcp_f32_e32 v87, v87
	v_mul_f32_e32 v86, v1, v1
	v_mul_f32_e32 v88, v82, v82
	v_mul_f32_e32 v86, 0xbf38aa3b, v86
	v_mul_f32_e32 v88, 0xbf38aa3b, v88
	s_waitcnt vmcnt(0)
	v_add_f32_e32 v29, v29, v0
	v_add_f32_e32 v0, v13, v0
	v_exp_f32_e32 v13, v86
	v_exp_f32_e32 v86, v88
	v_fmamk_f32 v88, v83, 0x3f07dc22, v126
	v_fmamk_f32 v89, v87, 0x3f07dc22, v126
	v_fmaak_f32 v88, v83, v88, 0x3f35f0e3
	v_fmaak_f32 v89, v87, v89, 0x3f35f0e3
	v_fmaak_f32 v88, v83, v88, 0xbe11a98e
	v_fmaak_f32 v89, v87, v89, 0xbe11a98e
	v_fmaak_f32 v88, v83, v88, 0x3e027906
	v_fmaak_f32 v89, v87, v89, 0x3e027906
	v_mul_f32_e32 v83, v83, v88
	v_mul_f32_e32 v87, v87, v89
	v_mul_f32_e32 v13, v13, v83
	v_mul_f32_e32 v83, v86, v87
	v_mul_f32_e32 v86, v13, v1
	v_fma_f32 v13, -v13, v1, v1
	v_cmp_gt_f32_e32 vcc, 0, v1
	v_mul_f32_e32 v87, v83, v82
	v_fma_f32 v83, -v83, v82, v82
	v_cndmask_b32_e32 v1, v13, v86, vcc
	v_cmp_gt_f32_e32 vcc, 0, v82
	v_mul_f32_e32 v29, v29, v1
	s_nop 0
	v_cndmask_b32_e32 v13, v83, v87, vcc
	v_mul_f32_e32 v13, v0, v13
	v_mul_f32_e32 v0, v13, v13
	v_fmac_f32_e32 v0, v29, v29
	s_nop 1
	s_waitcnt lgkmcnt(0)
	v_add_f32_dpp v0, v0, v0 quad_perm:[1,0,3,2] row_mask:0xf bank_mask:0xf
	s_nop 1
	s_waitcnt lgkmcnt(0)
	v_add_f32_dpp v0, v0, v0 quad_perm:[2,3,0,1] row_mask:0xf bank_mask:0xf
	s_nop 1
	s_waitcnt lgkmcnt(0)
	v_add_f32_dpp v0, v0, v0 row_half_mirror row_mask:0xf bank_mask:0xf
	s_nop 1
	s_waitcnt lgkmcnt(0)
	v_add_f32_dpp v0, v0, v0 row_mirror row_mask:0xf bank_mask:0xf
	ds_swizzle_b32 v1, v0 offset:swizzle(SWAP,16)
	s_and_saveexec_b64 s[4:5], s[0:1]
	s_cbranch_execz .LBB0_207
	s_waitcnt lgkmcnt(0)
	v_add_f32_e32 v0, v0, v1
	v_add_u32_e32 v1, s25, v121
	ds_write_b32 v1, v0 offset:32768
.LBB0_207:
	s_or_b64 exec, exec, s[4:5]
	s_waitcnt lgkmcnt(0)
	v_lshl_add_u64 v[0:1], v[80:81], 0, v[72:73]
	v_add_u32_e32 v0, s92, v122
	v_ashrrev_i32_e32 v1, 31, v0
	v_lshl_add_u64 v[0:1], v[0:1], 2, s[98:99]
	global_load_dword v0, v[0:1], off
	s_waitcnt vmcnt(0)
	v_mov_b32_e32 v82, v214
	v_lshlrev_b32_e32 v1, 16, v82
	v_and_b32_e32 v82, 0xffff0000, v82
	v_fma_f32 v83, |v1|, s87, 1.0
	v_fma_f32 v87, |v82|, s87, 1.0
	v_rcp_f32_e32 v83, v83
	v_rcp_f32_e32 v87, v87
	v_mul_f32_e32 v86, v1, v1
	v_mul_f32_e32 v88, v82, v82
	v_mul_f32_e32 v86, 0xbf38aa3b, v86
	v_mul_f32_e32 v88, 0xbf38aa3b, v88
	s_waitcnt vmcnt(0)
	v_add_f32_e32 v30, v30, v0
	v_add_f32_e32 v0, v14, v0
	v_exp_f32_e32 v14, v86
	v_exp_f32_e32 v86, v88
	v_fmamk_f32 v88, v83, 0x3f07dc22, v126
	v_fmamk_f32 v89, v87, 0x3f07dc22, v126
	v_fmaak_f32 v88, v83, v88, 0x3f35f0e3
	v_fmaak_f32 v89, v87, v89, 0x3f35f0e3
	v_fmaak_f32 v88, v83, v88, 0xbe11a98e
	v_fmaak_f32 v89, v87, v89, 0xbe11a98e
	v_fmaak_f32 v88, v83, v88, 0x3e027906
	v_fmaak_f32 v89, v87, v89, 0x3e027906
	v_mul_f32_e32 v83, v83, v88
	v_mul_f32_e32 v87, v87, v89
	v_mul_f32_e32 v14, v14, v83
	v_mul_f32_e32 v83, v86, v87
	v_mul_f32_e32 v86, v14, v1
	v_fma_f32 v14, -v14, v1, v1
	v_cmp_gt_f32_e32 vcc, 0, v1
	v_mul_f32_e32 v87, v83, v82
	v_fma_f32 v83, -v83, v82, v82
	v_cndmask_b32_e32 v1, v14, v86, vcc
	v_cmp_gt_f32_e32 vcc, 0, v82
	v_mul_f32_e32 v30, v30, v1
	s_nop 0
	v_cndmask_b32_e32 v14, v83, v87, vcc
	v_mul_f32_e32 v14, v0, v14
	v_mul_f32_e32 v0, v14, v14
	v_fmac_f32_e32 v0, v30, v30
	s_nop 1
	s_waitcnt lgkmcnt(0)
	v_add_f32_dpp v0, v0, v0 quad_perm:[1,0,3,2] row_mask:0xf bank_mask:0xf
	s_nop 1
	s_waitcnt lgkmcnt(0)
	v_add_f32_dpp v0, v0, v0 quad_perm:[2,3,0,1] row_mask:0xf bank_mask:0xf
	s_nop 1
	s_waitcnt lgkmcnt(0)
	v_add_f32_dpp v0, v0, v0 row_half_mirror row_mask:0xf bank_mask:0xf
	s_nop 1
	s_waitcnt lgkmcnt(0)
	v_add_f32_dpp v0, v0, v0 row_mirror row_mask:0xf bank_mask:0xf
	ds_swizzle_b32 v1, v0 offset:swizzle(SWAP,16)
	s_and_saveexec_b64 s[4:5], s[0:1]
	s_cbranch_execz .LBB0_209
	s_waitcnt lgkmcnt(0)
	v_add_f32_e32 v0, v0, v1
	v_add_u32_e32 v1, s25, v123
	ds_write_b32 v1, v0 offset:32768
.LBB0_209:
	s_or_b64 exec, exec, s[4:5]
	s_waitcnt lgkmcnt(0)
	v_lshl_add_u64 v[0:1], v[80:81], 0, v[74:75]
	v_add_u32_e32 v0, s92, v124
	v_ashrrev_i32_e32 v1, 31, v0
	v_lshl_add_u64 v[0:1], v[0:1], 2, s[98:99]
	global_load_dword v0, v[0:1], off
	s_waitcnt vmcnt(0)
	v_mov_b32_e32 v80, v215
	v_lshlrev_b32_e32 v1, 16, v80
	v_and_b32_e32 v80, 0xffff0000, v80
	v_fma_f32 v81, |v1|, s87, 1.0
	v_fma_f32 v83, |v80|, s87, 1.0
	v_rcp_f32_e32 v81, v81
	v_rcp_f32_e32 v83, v83
	v_mul_f32_e32 v82, v1, v1
	v_mul_f32_e32 v86, v80, v80
	v_mul_f32_e32 v82, 0xbf38aa3b, v82
	v_mul_f32_e32 v86, 0xbf38aa3b, v86
	s_waitcnt vmcnt(0)
	v_add_f32_e32 v31, v31, v0
	v_add_f32_e32 v0, v15, v0
	v_exp_f32_e32 v15, v82
	v_exp_f32_e32 v82, v86
	v_fmamk_f32 v86, v81, 0x3f07dc22, v126
	v_fmamk_f32 v87, v83, 0x3f07dc22, v126
	v_fmaak_f32 v86, v81, v86, 0x3f35f0e3
	v_fmaak_f32 v87, v83, v87, 0x3f35f0e3
	v_fmaak_f32 v86, v81, v86, 0xbe11a98e
	v_fmaak_f32 v87, v83, v87, 0xbe11a98e
	v_fmaak_f32 v86, v81, v86, 0x3e027906
	v_fmaak_f32 v87, v83, v87, 0x3e027906
	v_mul_f32_e32 v81, v81, v86
	v_mul_f32_e32 v83, v83, v87
	v_mul_f32_e32 v15, v15, v81
	v_mul_f32_e32 v81, v82, v83
	v_mul_f32_e32 v82, v15, v1
	v_fma_f32 v15, -v15, v1, v1
	v_cmp_gt_f32_e32 vcc, 0, v1
	v_mul_f32_e32 v83, v81, v80
	v_fma_f32 v81, -v81, v80, v80
	v_cndmask_b32_e32 v1, v15, v82, vcc
	v_cmp_gt_f32_e32 vcc, 0, v80
	v_mul_f32_e32 v31, v31, v1
	s_nop 0
	v_cndmask_b32_e32 v15, v81, v83, vcc
	v_mul_f32_e32 v15, v0, v15
	v_mul_f32_e32 v0, v15, v15
	v_fmac_f32_e32 v0, v31, v31
	s_nop 1
	s_waitcnt lgkmcnt(0)
	v_add_f32_dpp v0, v0, v0 quad_perm:[1,0,3,2] row_mask:0xf bank_mask:0xf
	s_nop 1
	s_waitcnt lgkmcnt(0)
	v_add_f32_dpp v0, v0, v0 quad_perm:[2,3,0,1] row_mask:0xf bank_mask:0xf
	s_nop 1
	s_waitcnt lgkmcnt(0)
	v_add_f32_dpp v0, v0, v0 row_half_mirror row_mask:0xf bank_mask:0xf
	s_nop 1
	s_waitcnt lgkmcnt(0)
	v_add_f32_dpp v0, v0, v0 row_mirror row_mask:0xf bank_mask:0xf
	ds_swizzle_b32 v1, v0 offset:swizzle(SWAP,16)
	s_and_saveexec_b64 s[4:5], s[0:1]
	s_cbranch_execz .LBB0_211
	s_waitcnt lgkmcnt(0)
	v_add_f32_e32 v0, v0, v1
	v_add_u32_e32 v1, s25, v125
	ds_write_b32 v1, v0 offset:32768
